# A/B of the static priority raise: waves 0-3 raised instead of waves 4-7 (flips removed), on top of v113
# speedup vs baseline: 1.0125x; 1.0125x over previous
; #define PG8_STAGE_B(bufoff, gbase) do { _Pragma("unroll") for (int _i = 0; _i < 2; ++_i) \
;         __builtin_amdgcn_global_load_lds((const unsigned*)((const char*)(gbase) + voffB[_i]), (LAS unsigned*)(lds + (bufoff) + ldsw + _i * 8192), 16, 0, 0); } while (0)
; #define PG8_STAGE_A(bufoff, AO, h, kb) do { _Pragma("unroll") for (int _i = 0; _i < 2; ++_i) \
;         __builtin_amdgcn_global_load_lds((const unsigned*)(S.A + (size_t)(AO)[h][_i] + (size_t)(kb)), (LAS unsigned*)(lds + (bufoff) + ldsw + _i * 8192), 16, 0, 0); } while (0)
; #define PG8_WAIT_V(n) asm volatile("s_waitcnt vmcnt(" #n ")" ::: "memory")
; #define PG8_BAR __builtin_amdgcn_s_barrier()
; template <class P>
; __device__ __forceinline__ void gemm_phase(LAS unsigned char* lds, const P& S) {
;     ...
;     for (int i = 0; i < 2; ++i) { int R, C; stage_rc(tid * 16 + i * 8192, R, C); const int Rb = P::PERM ? ((R & ~31) + perm32(R & 31)) : R;
;         RA[i] = R; CA[i] = C; if constexpr (P::BBLK) voffB[i] = (unsigned)((C >> 3) * S.NB + Rb) * 16u; else voffB[i] = (unsigned)(Rb * K + C) * 2u; }
;     const size_t kstep = (size_t)(BK * 2);
;     size_t kstepB = kstep; if constexpr (P::BBLK) kstepB = (size_t)128 * (size_t)S.NB;
;     const unsigned ldsw = (unsigned)wid * 1024u;
;     const int aoff = lds_byte(wr * 64 + fr, fq * 8), boff = lds_byte(wc * 32 + fr, fq * 8);
;     ...
; typedef int i32x2 __attribute__((ext_vector_type(2)));
;     ...
;     Unit cur, nxt; int ui = 0;
;     if (!S.next(0, cur)) return;
;     f32x4 acc[2][2][4][2];
; #pragma unroll
;     for (int a = 0; a < 2; ++a)
; #pragma unroll
;         for (int b = 0; b < 2; ++b)
; #pragma unroll
;             for (int m = 0; m < 4; ++m)
; #pragma unroll
;                 for (int n = 0; n < 2; ++n) acc[a][b][m][n] = (f32x4){0.f, 0.f, 0.f, 0.f};
;     i32x8 At[4], B0[2], B1[2];
;     unsigned ac[2][2], a2[2][2];
;     PG8_AOFF(ac, cur, 0);
;     const char* cB0 = S.bptr(cur, 0); const char* cB1 = S.bptr(cur, 1);
;     PG8_STAGE_B(PG8_SB(0, 0), cB0); PG8_STAGE_A(PG8_SA(0, 0), ac, 0, 0); PG8_STAGE_B(PG8_SB(0, 1), cB1); PG8_STAGE_A(PG8_SA(0, 1), ac, 1, 0);
;     if (wr == 1) PG8_BAR;
;     PG8_WAIT_V(4); PG8_BAR;
;     PG8_STAGE_B(PG8_SB(1, 0), cB0 + kstepB); PG8_STAGE_A(PG8_SA(1, 0), ac, 0, kstep); PG8_STAGE_B(PG8_SB(1, 1), cB1 + kstepB);
;     PG8_WAIT_V(6); PG8_BAR;
.LBB0_207:
	s_andn2_b64 vcc, exec, s[4:5]
	s_cbranch_vccnz .LBB0_227
	s_waitcnt vmcnt(16)
	v_mov_b32_e32 v14, v0
	s_cmpk_gt_i32 s80, 0x759
	v_readfirstlane_b32 s27, v14
	s_cbranch_scc1 .LBB0_227
	s_ashr_i32 s2, s80, 31
	s_lshr_b32 s2, s2, 29
	s_add_i32 s2, s80, s2
	s_and_b32 s3, s2, -8
	s_sub_i32 s3, s80, s3
	s_cmp_lt_i32 s3, 0
	s_movk_i32 s28, 0xe9
	v_ashrrev_i32_e32 v1, 31, v14
	s_cselect_b32 s4, s28, 0xe8
	v_lshrrev_b32_e32 v1, 26, v1
	s_mul_i32 s3, s4, s3
	s_ashr_i32 s2, s2, 3
	v_add_u32_e32 v1, v14, v1
	s_add_i32 s3, s3, s2
	v_ashrrev_i32_e32 v3, 6, v1
	v_bfe_i32 v1, v14, 27, 1
	s_mul_hi_i32 s2, s3, 0x8d3dcb09
	v_lshlrev_b32_e32 v2, 4, v14
	v_lshrrev_b32_e32 v1, 22, v1
	s_add_i32 s2, s2, s3
	v_add_u32_e32 v1, v2, v1
	s_lshr_b32 s4, s2, 31
	s_ashr_i32 s2, s2, 7
	v_and_b32_e32 v1, 0xfffffc00, v1
	s_add_i32 s2, s2, s4
	v_sub_u32_e32 v1, v2, v1
	v_add_u32_e32 v2, 0x2000, v2
	s_mul_i32 s4, s2, 0xe8
	v_ashrrev_i32_e32 v7, 31, v2
	s_sub_i32 s3, s3, s4
	v_lshrrev_b32_e32 v7, 22, v7
	s_sext_i32_i16 s4, s3
	v_add_u32_e32 v7, v2, v7
	s_bfe_u32 s4, s4, 0x3001c
	v_ashrrev_i32_e32 v7, 10, v7
	s_add_i32 s4, s3, s4
	v_mul_i32_i24_e32 v8, 0x400, v7
	s_sext_i32_i16 s5, s4
	s_and_b32 s4, s4, 0xfff8
	v_sub_u32_e32 v2, v2, v8
	s_sub_i32 s3, s3, s4
	v_lshrrev_b32_e32 v8, 4, v2
	s_sext_i32_i16 s3, s3
	s_lshl_b32 s2, s2, 3
	v_lshrrev_b32_e32 v4, 4, v1
	v_bitop3_b32 v2, v8, v2, 32 bitop3:0x6c
	s_ashr_i32 s5, s5, 3
	s_add_i32 s2, s2, s3
	s_add_i32 s3, s80, 0xfffff8c0
	s_add_i32 s4, s80, 0xfffff8b3
	v_bitop3_b32 v4, v4, v1, 32 bitop3:0x6c
	v_ashrrev_i32_e32 v9, 31, v2
	s_cmp_lt_u32 s3, 13
	v_ashrrev_i32_e32 v5, 31, v4
	v_lshrrev_b32_e32 v9, 26, v9
	s_cselect_b32 s6, s3, s4
	s_cmp_gt_u32 s3, 12
	v_lshrrev_b32_e32 v5, 26, v5
	v_lshlrev_b32_e32 v8, 3, v7
	v_add_u32_e32 v9, v2, v9
	s_cselect_b32 s3, 0x41, 64
	s_ashr_i32 s4, s27, 6
	v_add_u32_e32 v5, v4, v5
	v_and_b32_e32 v8, -16, v8
	v_ashrrev_i32_e32 v10, 6, v9
	s_ashr_i32 s8, s27, 8
	s_lshl_b32 s29, s4, 10
	v_ashrrev_i32_e32 v6, 6, v5
	v_add_u32_e32 v150, v10, v8
	v_and_b32_e32 v8, 0xc0, v9
	v_and_b32_e32 v5, 0xc0, v5
	s_cmpk_lt_i32 s80, 0x740
	v_sub_u32_e32 v2, v2, v8
	v_mov_b32_e32 v8, 1
	v_sub_u32_e32 v4, v4, v5
	v_lshlrev_b32_e32 v1, 3, v3
	s_cselect_b32 s46, s5, s6
	v_lshlrev_b32_e32 v7, 5, v7
	v_ashrrev_i16_sdwa v2, v8, sext(v2) dst_sel:DWORD dst_unused:UNUSED_PAD src0_sel:DWORD src1_sel:BYTE_0
	v_ashrrev_i16_sdwa v4, v8, sext(v4) dst_sel:DWORD dst_unused:UNUSED_PAD src0_sel:DWORD src1_sel:BYTE_0
	v_and_b32_e32 v5, 3, v10
	s_mov_b32 s5, 0xfffe0
	v_lshrrev_b32_e32 v8, 2, v150
	v_lshlrev_b32_e32 v9, 1, v150
	v_and_b32_e32 v1, -16, v1
	v_and_b32_e32 v7, 32, v7
	v_bfe_i32 v2, v2, 0, 16
	v_and_or_b32 v5, v150, s5, v5
	v_and_b32_e32 v8, 4, v8
	v_and_b32_e32 v9, 24, v9
	v_add_u32_e32 v1, v6, v1
	s_cselect_b32 s45, s2, s3
	s_add_u32 s2, s86, 0x33000000
	v_or3_b32 v5, v5, v8, v9
	v_add_lshl_u32 v151, v7, v2, 1
	s_addc_u32 s3, s87, 0
	v_lshlrev_b32_e32 v3, 5, v3
	v_lshl_add_u32 v130, v5, 12, v151
	v_and_b32_e32 v2, 3, v6
	v_lshrrev_b32_e32 v5, 2, v1
	v_lshlrev_b32_e32 v6, 1, v1
	s_add_u32 s30, s86, 0x800000
	v_and_b32_e32 v3, 32, v3
	v_bfe_i32 v4, v4, 0, 16
	v_and_or_b32 v2, v1, s5, v2
	v_and_b32_e32 v5, 4, v5
	v_and_b32_e32 v6, 24, v6
	s_addc_u32 s31, s87, 0
	v_or3_b32 v2, v2, v5, v6
	v_add_lshl_u32 v152, v3, v4, 1
	s_lshl_b32 s5, s45, 8
	s_lshl_b32 s6, s46, 8
	v_lshl_add_u32 v132, v2, 12, v152
	v_add_u32_e32 v2, s5, v1
	s_ashr_i32 s7, s6, 31
	v_lshl_add_u32 v136, v2, 12, v152
	v_add_u32_e32 v2, s5, v150
	s_bitset1_b32 s5, 7
	s_lshl_b64 s[10:11], s[6:7], 12
	s_add_u32 s18, s30, s10
	s_addc_u32 s19, s31, s11
	s_add_i32 s33, s29, 0
	s_bitset1_b32 s6, 7
	s_add_i32 m0, s33, 0x10000
	s_ashr_i32 s7, s6, 31
	global_load_lds_dwordx4 v132, s[18:19]
	s_add_i32 m0, s33, 0x12000
	s_lshl_b64 s[6:7], s[6:7], 12
	global_load_lds_dwordx4 v130, s[18:19]
	s_mov_b32 m0, s33
	s_add_i32 s34, s33, 0x2000
	v_lshl_add_u32 v138, v2, 12, v151
	global_load_lds_dwordx4 v136, s[2:3]
	s_mov_b32 m0, s34
	s_add_u32 s20, s30, s6
	global_load_lds_dwordx4 v138, s[2:3]
	s_addc_u32 s21, s31, s7
	s_add_i32 m0, s33, 0x14000
	v_add_u32_e32 v2, s5, v1
	global_load_lds_dwordx4 v132, s[20:21]
	s_add_i32 m0, s33, 0x16000
	s_add_i32 s35, s33, 0x4000
	v_lshl_add_u32 v140, v2, 12, v152
	v_add_u32_e32 v2, s5, v150
	global_load_lds_dwordx4 v130, s[20:21]
	s_mov_b32 m0, s35
	s_add_i32 s36, s33, 0x6000
	v_lshl_add_u32 v142, v2, 12, v151
	global_load_lds_dwordx4 v140, s[2:3]
	s_mov_b32 m0, s36
	v_mov_b32_e32 v135, 0
	global_load_lds_dwordx4 v142, s[2:3]
	v_mov_b32_e32 v133, v135
	v_mov_b32_e32 v131, v135
	v_mov_b32_e32 v137, v135
	v_mov_b32_e32 v139, v135
	s_mov_b32 s37, 0
	v_lshl_add_u64 v[12:13], s[18:19], 0, v[132:133]
	v_lshl_add_u64 v[10:11], s[18:19], 0, v[130:131]
	v_lshl_add_u64 v[8:9], s[2:3], 0, v[136:137]
	v_lshl_add_u64 v[6:7], s[2:3], 0, v[138:139]
	v_lshl_add_u64 v[4:5], s[20:21], 0, v[132:133]
	s_cmp_lg_u32 s8, 1
	v_lshl_add_u64 v[2:3], s[20:21], 0, v[130:131]
	s_setprio 1
	s_cbranch_scc1 .LBB0_211
	s_setprio 0
	s_barrier

; #define PG8_STAGE_B(bufoff, gbase) do { _Pragma("unroll") for (int _i = 0; _i < 2; ++_i) \
;         __builtin_amdgcn_global_load_lds((const unsigned*)((const char*)(gbase) + voffB[_i]), (LAS unsigned*)(lds + (bufoff) + ldsw + _i * 8192), 16, 0, 0); } while (0)
; #define PG8_WAIT_V(n) asm volatile("s_waitcnt vmcnt(" #n ")" ::: "memory")
; #define PG8_BAR __builtin_amdgcn_s_barrier()
; template <class P>
; __device__ __forceinline__ void gemm_phase(LAS unsigned char* lds, const P& S) {
;     int tid = threadIdx.x; asm volatile("" : "+v"(tid));
;     const int wid = __builtin_amdgcn_readfirstlane(tid >> 6), lane = tid & 63, wr = wid >> 2, wc = wid & 3, fr = lane & 15, fq = lane >> 4;
;     const int K = S.K, nt = K / BK;
;     unsigned voffB[2]; int RA[2], CA[2];
; #pragma unroll
;     for (int i = 0; i < 2; ++i) { int R, C; stage_rc(tid * 16 + i * 8192, R, C); const int Rb = P::PERM ? ((R & ~31) + perm32(R & 31)) : R;
;         RA[i] = R; CA[i] = C; if constexpr (P::BBLK) voffB[i] = (unsigned)((C >> 3) * S.NB + Rb) * 16u; else voffB[i] = (unsigned)(Rb * K + C) * 2u; }
;     const size_t kstep = (size_t)(BK * 2);
;     size_t kstepB = kstep; if constexpr (P::BBLK) kstepB = (size_t)128 * (size_t)S.NB;
;     const unsigned ldsw = (unsigned)wid * 1024u;
;     const int aoff = lds_byte(wr * 64 + fr, fq * 8), boff = lds_byte(wc * 32 + fr, fq * 8);
;     ...
; typedef int i32x2 __attribute__((ext_vector_type(2)));
;     ...
;     Unit cur, nxt; int ui = 0;
;     if (!S.next(0, cur)) return;
;     f32x4 acc[2][2][4][2];
; #pragma unroll
;     for (int a = 0; a < 2; ++a)
; #pragma unroll
;         for (int b = 0; b < 2; ++b)
; #pragma unroll
;             for (int m = 0; m < 4; ++m)
; #pragma unroll
;                 for (int n = 0; n < 2; ++n) acc[a][b][m][n] = (f32x4){0.f, 0.f, 0.f, 0.f};
;     i32x8 At[4], B0[2], B1[2];
;     unsigned ac[2][2], a2[2][2];
;     PG8_AOFF(ac, cur, 0);
;     const char* cB0 = S.bptr(cur, 0); const char* cB1 = S.bptr(cur, 1);
;     PG8_STAGE_B(PG8_SB(0, 0), cB0); PG8_STAGE_A(PG8_SA(0, 0), ac, 0, 0); PG8_STAGE_B(PG8_SB(0, 1), cB1); PG8_STAGE_A(PG8_SA(0, 1), ac, 1, 0);
;     if (wr == 1) PG8_BAR;
;     PG8_WAIT_V(4); PG8_BAR;
;     PG8_STAGE_B(PG8_SB(1, 0), cB0 + kstepB); PG8_STAGE_A(PG8_SA(1, 0), ac, 0, kstep); PG8_STAGE_B(PG8_SB(1, 1), cB1 + kstepB);
;     PG8_WAIT_V(6); PG8_BAR;
.LBB0_846:
	s_cmp_lt_i32 s68, 8
	s_cselect_b64 s[0:1], -1, 0
	s_and_b64 s[2:3], s[0:1], s[4:5]
	s_andn2_b64 vcc, exec, s[2:3]
	s_cbranch_vccnz .LBB0_867
	s_waitcnt vmcnt(0)
	v_mov_b32_e32 v14, v0
	s_cmpk_gt_i32 s80, 0x1ff
	s_nop 0
	v_readfirstlane_b32 s19, v14
	s_cbranch_scc1 .LBB0_867
	v_ashrrev_i32_e32 v1, 31, v14
	v_lshrrev_b32_e32 v1, 26, v1
	v_add_u32_e32 v1, v14, v1
	v_ashrrev_i32_e32 v3, 6, v1
	v_bfe_i32 v1, v14, 27, 1
	v_lshlrev_b32_e32 v2, 4, v14
	v_lshrrev_b32_e32 v1, 22, v1
	v_add_u32_e32 v1, v2, v1
	v_and_b32_e32 v1, 0xfffffc00, v1
	v_sub_u32_e32 v1, v2, v1
	v_add_u32_e32 v2, 0x2000, v2
	v_ashrrev_i32_e32 v7, 31, v2
	v_lshrrev_b32_e32 v7, 22, v7
	v_add_u32_e32 v7, v2, v7
	v_ashrrev_i32_e32 v7, 10, v7
	v_mul_i32_i24_e32 v8, 0x400, v7
	v_sub_u32_e32 v2, v2, v8
	v_lshrrev_b32_e32 v8, 4, v2
	v_bitop3_b32 v2, v8, v2, 32 bitop3:0x6c
	v_ashrrev_i32_e32 v9, 31, v2
	v_lshrrev_b32_e32 v9, 26, v9
	v_lshrrev_b32_e32 v4, 4, v1
	v_lshlrev_b32_e32 v8, 3, v7
	v_add_u32_e32 v9, v2, v9
	v_bitop3_b32 v4, v4, v1, 32 bitop3:0x6c
	v_and_b32_e32 v8, -16, v8
	v_ashrrev_i32_e32 v10, 6, v9
	v_ashrrev_i32_e32 v5, 31, v4
	v_add_u32_e32 v200, v10, v8
	v_and_b32_e32 v8, 0xc0, v9
	v_lshrrev_b32_e32 v5, 26, v5
	v_sub_u32_e32 v2, v2, v8
	v_mov_b32_e32 v8, 1
	s_waitcnt lgkmcnt(0)
	s_add_u32 s2, s86, 0x5d000000
	v_lshlrev_b32_e32 v1, 3, v3
	v_add_u32_e32 v5, v4, v5
	v_lshlrev_b32_e32 v7, 5, v7
	v_ashrrev_i16_sdwa v2, v8, sext(v2) dst_sel:DWORD dst_unused:UNUSED_PAD src0_sel:DWORD src1_sel:BYTE_0
	s_addc_u32 s3, s87, 0
	v_and_b32_e32 v1, -16, v1
	v_ashrrev_i32_e32 v6, 6, v5
	v_and_b32_e32 v7, 32, v7
	v_bfe_i32 v2, v2, 0, 16
	v_and_b32_e32 v5, 0xc0, v5
	s_add_u32 s33, s86, 0x2600000
	v_add_u32_e32 v1, v6, v1
	v_sub_u32_e32 v4, v4, v5
	v_and_b32_e32 v5, 3, v10
	s_mov_b32 s4, 0xfffe0
	v_add_lshl_u32 v201, v7, v2, 1
	v_and_b32_e32 v2, 3, v6
	s_addc_u32 s38, s87, 0
	v_and_or_b32 v5, v200, s4, v5
	v_and_or_b32 v2, v1, s4, v2
	s_ashr_i32 s4, s80, 31
	s_lshr_b32 s4, s4, 29
	s_add_i32 s4, s80, s4
	s_ashr_i32 s5, s4, 3
	s_and_b32 s4, s4, -8
	s_ashr_i32 s17, s19, 6
	s_sub_i32 s4, s80, s4
	s_ashr_i32 s16, s19, 8
	s_lshl_b32 s39, s17, 10
	s_lshl_b32 s7, s4, 6
	s_mul_i32 s6, s4, 0x41
	s_cmp_lt_i32 s4, 0
	s_cselect_b32 s4, s6, s7
	s_add_i32 s4, s4, s5
	s_ashr_i32 s5, s4, 31
	s_lshr_b32 s5, s5, 26
	s_add_i32 s5, s4, s5
	s_ashr_i32 s6, s5, 6
	s_andn2_b32 s5, s5, 63
	s_sub_i32 s4, s4, s5
	s_bfe_i32 s5, s4, 0x80000
	s_bfe_u32 s5, s5, 0x3000c
	v_ashrrev_i16_sdwa v4, v8, sext(v4) dst_sel:DWORD dst_unused:UNUSED_PAD src0_sel:DWORD src1_sel:BYTE_0
	v_lshrrev_b32_e32 v8, 2, v200
	v_lshlrev_b32_e32 v9, 1, v200
	s_add_i32 s5, s4, s5
	v_and_b32_e32 v8, 4, v8
	v_and_b32_e32 v9, 24, v9
	s_bfe_i32 s7, s5, 0x80000
	s_and_b32 s5, s5, 0xf8
	v_or3_b32 v5, v5, v8, v9
	s_sub_i32 s4, s4, s5
	v_lshlrev_b32_e32 v3, 5, v3
	v_lshl_add_u32 v154, v5, 12, v201
	v_lshrrev_b32_e32 v5, 2, v1
	v_lshlrev_b32_e32 v6, 1, v1
	s_lshl_b32 s6, s6, 3
	s_sext_i32_i8 s4, s4
	v_and_b32_e32 v3, 32, v3
	v_bfe_i32 v4, v4, 0, 16
	v_and_b32_e32 v5, 4, v5
	v_and_b32_e32 v6, 24, v6
	s_add_i32 s51, s6, s4
	v_or3_b32 v2, v2, v5, v6
	v_add_lshl_u32 v209, v3, v4, 1
	s_lshl_b32 s4, s51, 8
	v_lshl_add_u32 v156, v2, 12, v209
	v_add_u32_e32 v2, s4, v1
	s_sext_i32_i16 s7, s7
	v_lshl_add_u32 v130, v2, 12, v209
	v_add_u32_e32 v2, s4, v200
	s_bitset1_b32 s4, 7
	s_ashr_i32 s52, s7, 3
	v_lshl_add_u32 v132, v2, 12, v201
	v_add_u32_e32 v2, s4, v1
	v_lshl_add_u32 v134, v2, 12, v209
	v_add_u32_e32 v2, s4, v200
	s_lshl_b32 s4, s52, 8
	s_ashr_i32 s5, s4, 31
	s_lshl_b64 s[6:7], s[4:5], 12
	s_add_u32 s28, s33, s6
	s_addc_u32 s29, s38, s7
	s_add_i32 s40, s39, 0
	s_bitset1_b32 s4, 7
	s_add_i32 m0, s40, 0x10000
	s_ashr_i32 s5, s4, 31
	global_load_lds_dwordx4 v156, s[28:29]
	s_add_i32 m0, s40, 0x12000
	s_lshl_b64 s[4:5], s[4:5], 12
	global_load_lds_dwordx4 v154, s[28:29]
	s_mov_b32 m0, s40
	s_add_i32 s41, s40, 0x2000
	global_load_lds_dwordx4 v130, s[2:3]
	s_mov_b32 m0, s41
	s_add_u32 s30, s33, s4
	global_load_lds_dwordx4 v132, s[2:3]
	s_addc_u32 s31, s38, s5
	s_add_i32 m0, s40, 0x14000
	s_add_i32 s42, s40, 0x4000
	global_load_lds_dwordx4 v156, s[30:31]
	s_add_i32 m0, s40, 0x16000
	s_add_i32 s43, s40, 0x6000
	global_load_lds_dwordx4 v154, s[30:31]
	s_mov_b32 m0, s42
	v_lshl_add_u32 v136, v2, 12, v201
	global_load_lds_dwordx4 v134, s[2:3]
	s_mov_b32 m0, s43
	s_load_dwordx4 s[4:7], s[88:89], 0x20
	global_load_lds_dwordx4 v136, s[2:3]
	v_mov_b32_e32 v159, 0
	v_mov_b32_e32 v157, v159
	v_mov_b32_e32 v155, v159
	v_mov_b32_e32 v131, v159
	v_mov_b32_e32 v133, v159
	s_mov_b32 s44, 0
	v_lshl_add_u64 v[12:13], s[28:29], 0, v[156:157]
	v_lshl_add_u64 v[10:11], s[28:29], 0, v[154:155]
	v_lshl_add_u64 v[8:9], s[2:3], 0, v[130:131]
	v_lshl_add_u64 v[6:7], s[2:3], 0, v[132:133]
	v_lshl_add_u64 v[4:5], s[30:31], 0, v[156:157]
	s_cmp_lg_u32 s16, 1
	v_lshl_add_u64 v[2:3], s[30:31], 0, v[154:155]
	s_setprio 1
	s_cbranch_scc1 .LBB0_850
	s_setprio 0
	s_barrier

; #define PG8_STAGE_B(bufoff, gbase) do { _Pragma("unroll") for (int _i = 0; _i < 2; ++_i) \
;         __builtin_amdgcn_global_load_lds((const unsigned*)((const char*)(gbase) + voffB[_i]), (LAS unsigned*)(lds + (bufoff) + ldsw + _i * 8192), 16, 0, 0); } while (0)
; #define PG8_STAGE_A(bufoff, AO, h, kb) do { _Pragma("unroll") for (int _i = 0; _i < 2; ++_i) \
;         __builtin_amdgcn_global_load_lds((const unsigned*)(S.A + (size_t)(AO)[h][_i] + (size_t)(kb)), (LAS unsigned*)(lds + (bufoff) + ldsw + _i * 8192), 16, 0, 0); } while (0)
; #define PG8_WAIT_V(n) asm volatile("s_waitcnt vmcnt(" #n ")" ::: "memory")
; #define PG8_BAR __builtin_amdgcn_s_barrier()
; #define PG8_AOFF(AO, u, ord) do { _Pragma("unroll") for (int _h = 0; _h < 2; ++_h) _Pragma("unroll") for (int _i = 0; _i < 2; ++_i) \
;         (AO)[_h][_i] = (unsigned)((size_t)S.arow_i((ord), (u), _h * HALF + RA[_i]) * (size_t)K + (size_t)CA[_i]) * 2u; } while (0)
; template <class P>
; __device__ __forceinline__ void gemm_phase(LAS unsigned char* lds, const P& S) {
;     ...
;     Unit cur, nxt; int ui = 0;
;     if (!S.next(0, cur)) return;
;     f32x4 acc[2][2][4][2];
; #pragma unroll
;     for (int a = 0; a < 2; ++a)
; #pragma unroll
;         for (int b = 0; b < 2; ++b)
; #pragma unroll
;             for (int m = 0; m < 4; ++m)
; #pragma unroll
;                 for (int n = 0; n < 2; ++n) acc[a][b][m][n] = (f32x4){0.f, 0.f, 0.f, 0.f};
;     i32x8 At[4], B0[2], B1[2];
;     unsigned ac[2][2], a2[2][2];
;     PG8_AOFF(ac, cur, 0);
;     const char* cB0 = S.bptr(cur, 0); const char* cB1 = S.bptr(cur, 1);
;     PG8_STAGE_B(PG8_SB(0, 0), cB0); PG8_STAGE_A(PG8_SA(0, 0), ac, 0, 0); PG8_STAGE_B(PG8_SB(0, 1), cB1); PG8_STAGE_A(PG8_SA(0, 1), ac, 1, 0);
;     if (wr == 1) PG8_BAR;
;     PG8_WAIT_V(4); PG8_BAR;
;     __device__ __forceinline__ bool next(int i, Unit& u) const {
;         const int NT = ps[32] / 256, NU = NT * 16, L = i * G + c; if (L >= NU) return false;
;         pg8::tile_order(L, NT, 16, u.pm, u.pn); u.e = moe_tile_expert(ps, u.pm); return true;
;     }
;     __device__ __forceinline__ const char* bptr(const Unit& u, int half) const { return (half ? Wu : Wg) + (size_t)u.e * D * D + (size_t)(u.pn * 128) * 16; }
;     __device__ __forceinline__ unsigned arow_i(int ord, const Unit&, int r) const { return (unsigned)gtab[ord * 256 + r]; }
.LBB0_1038:
	s_or_b64 exec, exec, s[2:3]
	s_add_i32 s2, 0, 0x25100
	v_mov_b32_e32 v3, v0
	v_mov_b32_e32 v1, s2
	s_waitcnt lgkmcnt(0)
	s_barrier
	ds_read_b32 v1, v1
	v_readfirstlane_b32 s15, v3
	s_waitcnt lgkmcnt(0)
	v_readfirstlane_b32 s2, v1
	s_ashr_i32 s3, s2, 31
	s_lshr_b32 s3, s3, 24
	s_add_i32 s2, s2, s3
	s_ashr_i32 s5, s2, 8
	s_lshl_b32 s2, s5, 4
	s_cmp_lt_i32 s80, s2
	s_cbranch_scc0 .LBB0_1064
	v_ashrrev_i32_e32 v1, 31, v3
	v_lshrrev_b32_e32 v1, 26, v1
	v_add_u32_e32 v1, v3, v1
	v_ashrrev_i32_e32 v4, 6, v1
	v_bfe_i32 v1, v3, 27, 1
	v_lshlrev_b32_e32 v2, 4, v3
	v_lshrrev_b32_e32 v1, 22, v1
	v_add_u32_e32 v1, v2, v1
	v_and_b32_e32 v1, 0xfffffc00, v1
	v_sub_u32_e32 v1, v2, v1
	v_add_u32_e32 v2, 0x2000, v2
	v_ashrrev_i32_e32 v8, 31, v2
	v_lshrrev_b32_e32 v8, 22, v8
	v_add_u32_e32 v8, v2, v8
	v_ashrrev_i32_e32 v8, 10, v8
	v_mul_i32_i24_e32 v9, 0x400, v8
	v_sub_u32_e32 v2, v2, v9
	v_lshrrev_b32_e32 v9, 4, v2
	v_bitop3_b32 v2, v9, v2, 32 bitop3:0x6c
	v_ashrrev_i32_e32 v10, 31, v2
	v_lshrrev_b32_e32 v10, 26, v10
	v_lshrrev_b32_e32 v5, 4, v1
	v_lshlrev_b32_e32 v9, 3, v8
	v_add_u32_e32 v10, v2, v10
	v_bitop3_b32 v5, v5, v1, 32 bitop3:0x6c
	v_and_b32_e32 v9, -16, v9
	v_ashrrev_i32_e32 v11, 6, v10
	s_ashr_i32 s6, s15, 6
	v_ashrrev_i32_e32 v6, 31, v5
	v_add_u32_e32 v184, v11, v9
	v_and_b32_e32 v9, 0xc0, v10
	s_ashr_i32 s8, s15, 8
	v_lshrrev_b32_e32 v6, 26, v6
	s_lshl_b32 s17, s6, 10
	v_lshlrev_b32_e32 v8, 5, v8
	v_sub_u32_e32 v2, v2, v9
	v_mov_b32_e32 v9, 1
	v_add_u32_e32 v6, v5, v6
	s_add_u32 s33, s86, 0x3000000
	v_and_b32_e32 v8, 32, v8
	v_ashrrev_i16_sdwa v2, v9, sext(v2) dst_sel:DWORD dst_unused:UNUSED_PAD src0_sel:DWORD src1_sel:BYTE_0
	v_lshlrev_b32_e32 v1, 3, v4
	s_addc_u32 s40, s87, 0
	v_add_u32_sdwa v8, v8, sext(v2) dst_sel:DWORD dst_unused:UNUSED_PAD src0_sel:DWORD src1_sel:WORD_0
	v_lshlrev_b32_e32 v2, 5, v4
	v_and_b32_e32 v4, 0xc0, v6
	s_add_u32 s2, s86, 0x69000000
	v_sub_u32_e32 v4, v5, v4
	s_addc_u32 s3, s87, 0
	v_and_b32_e32 v2, 32, v2
	v_ashrrev_i16_sdwa v4, v9, sext(v4) dst_sel:DWORD dst_unused:UNUSED_PAD src0_sel:DWORD src1_sel:BYTE_0
	v_ashrrev_i32_e32 v7, 6, v6
	s_add_u32 s41, s86, 0x13000000
	v_add_u32_sdwa v4, v2, sext(v4) dst_sel:DWORD dst_unused:UNUSED_PAD src0_sel:DWORD src1_sel:WORD_0
	v_and_b32_e32 v2, 3, v11
	s_mov_b32 s14, 0xfffffe0
	v_lshlrev_b32_e32 v5, 1, v184
	v_lshrrev_b32_e32 v6, 2, v184
	s_addc_u32 s42, s87, 0
	s_ashr_i32 s7, s80, 31
	v_and_or_b32 v2, v184, s14, v2
	v_and_b32_e32 v5, 24, v5
	v_and_b32_e32 v6, 4, v6
	v_and_b32_e32 v1, -16, v1
	s_lshr_b32 s7, s7, 29
	v_or3_b32 v2, v2, v5, v6
	v_lshlrev_b32_e32 v5, 8, v8
	v_add_u32_e32 v1, v7, v1
	s_add_i32 s7, s80, s7
	v_and_b32_e32 v5, 0xffff800, v5
	s_ashr_i32 s9, s7, 3
	s_and_b32 s7, s7, -8
	v_add_lshl_u32 v154, v2, v5, 4
	v_and_b32_e32 v2, 3, v7
	v_lshlrev_b32_e32 v5, 1, v1
	v_lshrrev_b32_e32 v6, 2, v1
	s_sub_i32 s7, s80, s7
	v_and_or_b32 v2, v1, s14, v2
	v_and_b32_e32 v5, 24, v5
	v_and_b32_e32 v6, 4, v6
	v_or3_b32 v2, v2, v5, v6
	v_mov_b32_e32 v5, s7
	v_alignbit_b32 v5, s5, v5, 31
	v_lshlrev_b32_e32 v6, 8, v4
	v_readfirstlane_b32 s14, v5
	s_mul_i32 s7, s14, s7
	s_add_i32 s7, s7, s9
	s_ashr_i32 s9, s7, 31
	s_lshr_b32 s9, s9, 25
	s_add_i32 s9, s7, s9
	s_ashr_i32 s14, s9, 7
	s_lshl_b32 s14, s14, 3
	s_sub_i32 s5, s5, s14
	s_min_i32 s5, s5, 8
	s_abs_i32 s16, s5
	v_cvt_f32_u32_e32 v5, s16
	v_and_b32_e32 v6, 0xffff800, v6
	v_add_lshl_u32 v156, v2, v6, 4
	s_sub_i32 s19, 0, s16
	v_rcp_iflag_f32_e32 v2, v5
	s_and_b32 s9, s9, 0xffffff80
	s_sub_i32 s7, s7, s9
	s_abs_i32 s18, s7
	v_mul_f32_e32 v2, 0x4f7ffffe, v2
	v_cvt_u32_f32_e32 v2, v2
	s_xor_b32 s9, s7, s5
	s_ashr_i32 s9, s9, 31
	v_lshlrev_b32_e32 v5, 2, v1
	v_readfirstlane_b32 s20, v2
	s_mul_i32 s19, s19, s20
	s_mul_hi_u32 s19, s20, s19
	s_add_i32 s20, s20, s19
	s_mul_hi_u32 s19, s18, s20
	s_mul_i32 s20, s19, s16
	s_sub_i32 s18, s18, s20
	s_add_i32 s20, s19, 1
	s_sub_i32 s21, s18, s16
	s_cmp_ge_u32 s18, s16
	s_cselect_b32 s19, s20, s19
	s_cselect_b32 s18, s21, s18
	s_add_i32 s20, s19, 1
	s_cmp_ge_u32 s18, s16
	s_cselect_b32 s16, s20, s19
	s_xor_b32 s16, s16, s9
	s_sub_i32 s28, s16, s9
	s_mul_i32 s5, s28, s5
	s_sub_i32 s5, s7, s5
	s_add_i32 s57, s5, s14
	s_lshl_b32 s5, s57, 2
	s_add_i32 s5, s5, 0
	v_lshlrev_b32_e32 v7, 2, v184
	s_add_i32 s5, s5, 0x25140
	v_add_u32_e32 v6, s4, v5
	v_add_u32_e32 v9, s4, v7
	s_add_i32 s4, 0, 0x20200
	v_mov_b32_e32 v2, s5
	v_add_u32_e32 v5, s4, v5
	v_add_u32_e32 v7, s4, v7
	ds_read_b32 v2, v2
	ds_read_b32 v6, v6
	ds_read_b32 v9, v9
	ds_read_b32 v5, v5
	ds_read_b32 v7, v7
	s_waitcnt lgkmcnt(4)
	v_readfirstlane_b32 s4, v2
	s_ashr_i32 s5, s4, 31
	s_lshl_b64 s[4:5], s[4:5], 22
	s_add_u32 s7, s33, s4
	s_addc_u32 s9, s40, s5
	s_lshl_b32 s18, s28, 7
	s_ashr_i32 s19, s18, 31
	s_lshl_b64 s[18:19], s[18:19], 4
	s_add_u32 s30, s7, s18
	s_addc_u32 s31, s9, s19
	s_add_u32 s4, s41, s4
	s_addc_u32 s5, s42, s5
	s_add_i32 s43, s17, 0
	s_add_i32 m0, s43, 0x10000
	v_lshlrev_b32_e32 v185, 1, v4
	global_load_lds_dwordx4 v156, s[30:31]
	s_add_i32 m0, s43, 0x12000
	s_waitcnt lgkmcnt(0)
	v_lshl_add_u32 v166, v6, 11, v185
	v_lshlrev_b32_e32 v186, 1, v8
	global_load_lds_dwordx4 v154, s[30:31]
	s_mov_b32 m0, s43
	s_add_i32 s44, s43, 0x2000
	v_lshl_add_u32 v172, v9, 11, v186
	global_load_lds_dwordx4 v166, s[2:3]
	s_mov_b32 m0, s44
	s_add_u32 s34, s4, s18
	global_load_lds_dwordx4 v172, s[2:3]
	s_addc_u32 s35, s5, s19
	s_add_i32 m0, s43, 0x14000
	s_add_i32 s45, s43, 0x4000
	global_load_lds_dwordx4 v156, s[34:35]
	s_add_i32 m0, s43, 0x16000
	v_lshl_add_u32 v170, v5, 11, v185
	global_load_lds_dwordx4 v154, s[34:35]
	s_mov_b32 m0, s45
	s_add_i32 s46, s43, 0x6000
	v_lshl_add_u32 v168, v7, 11, v186
	global_load_lds_dwordx4 v170, s[2:3]
	s_mov_b32 m0, s46
	v_mov_b32_e32 v159, 0
	global_load_lds_dwordx4 v168, s[2:3]
	v_mov_b32_e32 v167, v159
	v_mov_b32_e32 v173, v159
	v_mov_b32_e32 v157, v159
	v_mov_b32_e32 v155, v159
	v_lshl_add_u64 v[6:7], s[2:3], 0, v[166:167]
	s_cmp_lg_u32 s8, 1
	v_lshl_add_u64 v[4:5], s[2:3], 0, v[172:173]
	s_setprio 1
	s_cbranch_scc1 .LBB0_1041
	s_setprio 0
	s_barrier

; #define PG8_STAGE_B(bufoff, gbase) do { _Pragma("unroll") for (int _i = 0; _i < 2; ++_i) \
;         __builtin_amdgcn_global_load_lds((const unsigned*)((const char*)(gbase) + voffB[_i]), (LAS unsigned*)(lds + (bufoff) + ldsw + _i * 8192), 16, 0, 0); } while (0)
; #define PG8_STAGE_A(bufoff, AO, h, kb) do { _Pragma("unroll") for (int _i = 0; _i < 2; ++_i) \
;         __builtin_amdgcn_global_load_lds((const unsigned*)(S.A + (size_t)(AO)[h][_i] + (size_t)(kb)), (LAS unsigned*)(lds + (bufoff) + ldsw + _i * 8192), 16, 0, 0); } while (0)
; #define PG8_WAIT_V(n) asm volatile("s_waitcnt vmcnt(" #n ")" ::: "memory")
; #define PG8_BAR __builtin_amdgcn_s_barrier()
; #define PG8_AOFF(AO, u, ord) do { _Pragma("unroll") for (int _h = 0; _h < 2; ++_h) _Pragma("unroll") for (int _i = 0; _i < 2; ++_i) \
;         (AO)[_h][_i] = (unsigned)((size_t)S.arow_i((ord), (u), _h * HALF + RA[_i]) * (size_t)K + (size_t)CA[_i]) * 2u; } while (0)
;     __device__ __forceinline__ unsigned arow_i(int, const Unit& u, int r) const { return (unsigned)(u.pm * 256 + r); }
; template <class P>
; __device__ __forceinline__ void gemm_phase(LAS unsigned char* lds, const P& S) {
;     ...
;     Unit cur, nxt; int ui = 0;
;     if (!S.next(0, cur)) return;
;     f32x4 acc[2][2][4][2];
; #pragma unroll
;     for (int a = 0; a < 2; ++a)
; #pragma unroll
;         for (int b = 0; b < 2; ++b)
; #pragma unroll
;             for (int m = 0; m < 4; ++m)
; #pragma unroll
;                 for (int n = 0; n < 2; ++n) acc[a][b][m][n] = (f32x4){0.f, 0.f, 0.f, 0.f};
;     i32x8 At[4], B0[2], B1[2];
;     unsigned ac[2][2], a2[2][2];
;     PG8_AOFF(ac, cur, 0);
;     const char* cB0 = S.bptr(cur, 0); const char* cB1 = S.bptr(cur, 1);
;     PG8_STAGE_B(PG8_SB(0, 0), cB0); PG8_STAGE_A(PG8_SA(0, 0), ac, 0, 0); PG8_STAGE_B(PG8_SB(0, 1), cB1); PG8_STAGE_A(PG8_SA(0, 1), ac, 1, 0);
;     if (wr == 1) PG8_BAR;
;     PG8_WAIT_V(4); PG8_BAR;
;     __device__ __forceinline__ bool next(int i, Unit& u) const {
;         const int NT = ps[32] / 256, NU = NT * 8, L = i * G + c; if (L >= NU) return false;
;         pg8::tile_order(L, NT, 8, u.pm, u.pn); u.e = moe_tile_expert(ps, u.pm); return true;
;     }
;     __device__ __forceinline__ unsigned arow_i(int, const Unit& u, int r) const { return (unsigned)(u.pm * 256 + r); }
.LBB0_1114:
	s_cmp_lt_i32 s68, 11
	s_cselect_b64 s[0:1], -1, 0
	s_and_b64 s[2:3], s[0:1], s[2:3]
	s_andn2_b64 vcc, exec, s[2:3]
	s_cbranch_vccnz .LBB0_1133
	s_add_i32 s2, 0, 0x25100
	s_waitcnt vmcnt(0)
	v_mov_b32_e32 v3, v0
	v_mov_b32_e32 v1, s2
	ds_read_b32 v1, v1
	v_readfirstlane_b32 s17, v3
	s_waitcnt lgkmcnt(0)
	v_readfirstlane_b32 s2, v1
	s_ashr_i32 s3, s2, 31
	s_lshr_b32 s3, s3, 24
	s_add_i32 s2, s2, s3
	s_ashr_i32 s4, s2, 8
	s_lshl_b32 s2, s4, 3
	s_cmp_ge_i32 s80, s2
	s_cbranch_scc1 .LBB0_1133
	v_ashrrev_i32_e32 v1, 31, v3
	v_lshrrev_b32_e32 v1, 26, v1
	v_add_u32_e32 v1, v3, v1
	v_ashrrev_i32_e32 v4, 6, v1
	v_bfe_i32 v1, v3, 27, 1
	v_lshlrev_b32_e32 v2, 4, v3
	v_lshrrev_b32_e32 v1, 22, v1
	v_add_u32_e32 v1, v2, v1
	v_and_b32_e32 v1, 0xfffffc00, v1
	v_sub_u32_e32 v1, v2, v1
	v_add_u32_e32 v2, 0x2000, v2
	v_ashrrev_i32_e32 v8, 31, v2
	v_lshrrev_b32_e32 v8, 22, v8
	v_add_u32_e32 v8, v2, v8
	v_ashrrev_i32_e32 v8, 10, v8
	s_add_u32 s2, s86, 0x37200000
	v_mul_i32_i24_e32 v9, 0x400, v8
	s_addc_u32 s3, s87, 0
	v_sub_u32_e32 v2, v2, v9
	s_add_u32 s19, s86, 0x23000000
	v_lshrrev_b32_e32 v9, 4, v2
	s_addc_u32 s33, s87, 0
	v_bitop3_b32 v2, v9, v2, 32 bitop3:0x6c
	s_ashr_i32 s5, s80, 31
	v_ashrrev_i32_e32 v10, 31, v2
	s_lshr_b32 s5, s5, 29
	v_lshrrev_b32_e32 v10, 26, v10
	s_add_i32 s5, s80, s5
	v_lshrrev_b32_e32 v5, 4, v1
	v_lshlrev_b32_e32 v9, 3, v8
	v_add_u32_e32 v10, v2, v10
	s_ashr_i32 s7, s5, 3
	s_and_b32 s5, s5, -8
	v_bitop3_b32 v5, v5, v1, 32 bitop3:0x6c
	v_and_b32_e32 v9, -16, v9
	v_ashrrev_i32_e32 v11, 6, v10
	s_sub_i32 s5, s80, s5
	v_ashrrev_i32_e32 v6, 31, v5
	v_add_u32_e32 v182, v11, v9
	v_and_b32_e32 v9, 0xc0, v10
	s_lshr_b32 s8, s5, 31
	v_lshrrev_b32_e32 v6, 26, v6
	v_lshlrev_b32_e32 v8, 5, v8
	v_sub_u32_e32 v2, v2, v9
	v_mov_b32_e32 v9, 1
	s_add_i32 s8, s4, s8
	v_add_u32_e32 v6, v5, v6
	v_and_b32_e32 v8, 32, v8
	v_ashrrev_i16_sdwa v2, v9, sext(v2) dst_sel:DWORD dst_unused:UNUSED_PAD src0_sel:DWORD src1_sel:BYTE_0
	s_mul_i32 s5, s8, s5
	v_lshlrev_b32_e32 v1, 3, v4
	v_add_u32_sdwa v8, v8, sext(v2) dst_sel:DWORD dst_unused:UNUSED_PAD src0_sel:DWORD src1_sel:WORD_0
	v_lshlrev_b32_e32 v2, 5, v4
	v_and_b32_e32 v4, 0xc0, v6
	s_add_i32 s5, s5, s7
	v_sub_u32_e32 v4, v5, v4
	s_ashr_i32 s7, s5, 31
	v_and_b32_e32 v2, 32, v2
	v_ashrrev_i16_sdwa v4, v9, sext(v4) dst_sel:DWORD dst_unused:UNUSED_PAD src0_sel:DWORD src1_sel:BYTE_0
	s_lshr_b32 s7, s7, 26
	v_ashrrev_i32_e32 v7, 6, v6
	v_add_u32_sdwa v4, v2, sext(v4) dst_sel:DWORD dst_unused:UNUSED_PAD src0_sel:DWORD src1_sel:WORD_0
	v_and_b32_e32 v2, 3, v11
	s_mov_b32 s9, 0xfffffe0
	v_lshlrev_b32_e32 v5, 1, v182
	v_lshrrev_b32_e32 v6, 2, v182
	s_add_i32 s7, s5, s7
	v_and_or_b32 v2, v182, s9, v2
	v_and_b32_e32 v5, 24, v5
	v_and_b32_e32 v6, 4, v6
	s_ashr_i32 s8, s7, 6
	v_or3_b32 v2, v2, v5, v6
	v_lshlrev_b32_e32 v5, 8, v8
	s_lshl_b32 s8, s8, 3
	v_and_b32_e32 v1, -16, v1
	v_and_b32_e32 v5, 0xffff800, v5
	s_sub_i32 s4, s4, s8
	v_add_u32_e32 v1, v7, v1
	v_add_lshl_u32 v154, v2, v5, 4
	v_and_b32_e32 v2, 3, v7
	s_min_i32 s4, s4, 8
	v_and_or_b32 v5, v1, s9, v2
	s_abs_i32 s9, s4
	v_cvt_f32_u32_e32 v6, s9
	v_lshlrev_b32_e32 v2, 1, v1
	v_and_b32_e32 v7, 24, v2
	v_lshrrev_b32_e32 v2, 2, v1
	v_and_b32_e32 v9, 4, v2
	v_rcp_iflag_f32_e32 v2, v6
	s_sub_i32 s12, 0, s9
	s_andn2_b32 s7, s7, 63
	s_sub_i32 s5, s5, s7
	v_mul_f32_e32 v2, 0x4f7ffffe, v2
	v_cvt_u32_f32_e32 v2, v2
	s_abs_i32 s11, s5
	s_ashr_i32 s6, s17, 6
	s_xor_b32 s7, s5, s4
	v_readfirstlane_b32 s13, v2
	s_mul_i32 s12, s12, s13
	s_mul_hi_u32 s12, s13, s12
	s_add_i32 s13, s13, s12
	s_mul_hi_u32 s12, s11, s13
	s_mul_i32 s13, s12, s9
	s_sub_i32 s11, s11, s13
	s_ashr_i32 s10, s17, 8
	s_lshl_b32 s48, s6, 10
	s_ashr_i32 s7, s7, 31
	s_add_i32 s13, s12, 1
	s_sub_i32 s14, s11, s9
	s_cmp_ge_u32 s11, s9
	s_cselect_b32 s12, s13, s12
	s_cselect_b32 s11, s14, s11
	s_add_i32 s13, s12, 1
	s_cmp_ge_u32 s11, s9
	s_cselect_b32 s9, s13, s12
	s_xor_b32 s9, s9, s7
	s_sub_i32 s38, s9, s7
	s_mul_i32 s4, s38, s4
	s_sub_i32 s4, s5, s4
	s_add_i32 s65, s4, s8
	s_lshl_b32 s4, s65, 2
	s_add_i32 s4, s4, 0
	s_add_i32 s4, s4, 0x25140
	v_mov_b32_e32 v2, s4
	ds_read_b32 v2, v2
	v_lshlrev_b32_e32 v6, 8, v4
	v_or3_b32 v5, v5, v7, v9
	v_and_b32_e32 v6, 0xffff800, v6
	s_lshl_b32 s7, s65, 8
	s_waitcnt lgkmcnt(0)
	v_readfirstlane_b32 s4, v2
	v_add_lshl_u32 v156, v5, v6, 4
	s_ashr_i32 s5, s4, 31
	v_add_u32_e32 v5, s7, v1
	v_lshlrev_b32_e32 v183, 1, v4
	v_add_u32_e32 v4, s7, v182
	v_lshlrev_b32_e32 v184, 1, v8
	s_bitset1_b32 s7, 7
	v_lshl_add_u32 v164, v4, 11, v184
	v_add_u32_e32 v4, s7, v1
	s_lshl_b64 s[4:5], s[4:5], 22
	v_lshl_add_u32 v166, v4, 11, v183
	v_add_u32_e32 v4, s7, v182
	s_add_u32 s7, s19, s4
	s_addc_u32 s11, s33, s5
	s_lshl_b32 s4, s38, 8
	s_ashr_i32 s5, s4, 31
	s_lshl_b64 s[8:9], s[4:5], 4
	s_add_u32 s40, s7, s8
	s_addc_u32 s41, s11, s9
	s_add_i32 s49, s48, 0
	s_bitset1_b32 s4, 7
	s_add_i32 m0, s49, 0x10000
	s_ashr_i32 s5, s4, 31
	global_load_lds_dwordx4 v156, s[40:41]
	s_add_i32 m0, s49, 0x12000
	v_lshl_add_u32 v162, v5, 11, v183
	s_lshl_b64 s[4:5], s[4:5], 4
	global_load_lds_dwordx4 v154, s[40:41]
	s_mov_b32 m0, s49
	s_add_i32 s50, s49, 0x2000
	global_load_lds_dwordx4 v162, s[2:3]
	s_mov_b32 m0, s50
	s_add_u32 s42, s7, s4
	global_load_lds_dwordx4 v164, s[2:3]
	s_addc_u32 s43, s11, s5
	s_add_i32 m0, s49, 0x14000
	s_add_i32 s51, s49, 0x4000
	global_load_lds_dwordx4 v156, s[42:43]
	s_add_i32 m0, s49, 0x16000
	s_add_i32 s52, s49, 0x6000
	global_load_lds_dwordx4 v154, s[42:43]
	s_mov_b32 m0, s51
	v_lshl_add_u32 v168, v4, 11, v184
	global_load_lds_dwordx4 v166, s[2:3]
	s_mov_b32 m0, s52
	v_mov_b32_e32 v159, 0
	global_load_lds_dwordx4 v168, s[2:3]
	v_mov_b32_e32 v163, v159
	v_mov_b32_e32 v165, v159
	v_mov_b32_e32 v157, v159
	v_mov_b32_e32 v155, v159
	v_lshl_add_u64 v[6:7], s[2:3], 0, v[162:163]
	s_cmp_lg_u32 s10, 1
	v_lshl_add_u64 v[4:5], s[2:3], 0, v[164:165]
	s_setprio 1
	s_cbranch_scc1 .LBB0_1118
	s_setprio 0
	s_barrier
